# prep pack path: all 16 W1/W2-row loads hoisted to block start (issued with the inv_ms loads), consumed via v_mov
# baseline (speedup 1.0000x reference)
_Z11prep_kernelPKfPDv8_DF16_S0_S0_S0_S0_S0_S0_S0_S0_S0_S2_PfPDF16_S4_S3_:
	s_load_dwordx2 s[16:17], s[0:1], 0x50
	s_load_dwordx4 s[28:31], s[0:1], 0x0
	s_cmpk_gt_u32 s2, 0x1ff
	s_mov_b64 s[4:5], -1
	s_cbranch_scc1 .LBB0_3
	s_andn2_b64 vcc, exec, s[4:5]
	s_cbranch_vccz .LBB0_75

.LBB0_75:
	s_lshr_b32 s3, s2, 5
	s_waitcnt lgkmcnt(0)
	s_lshl_b32 s8, s3, 9
	s_mov_b32 s9, 0
	s_lshl_b64 s[4:5], s[8:9], 2
	s_add_u32 s4, s16, s4
	s_addc_u32 s5, s17, s5
	v_lshlrev_b32_e32 v1, 2, v0
	global_load_dword v2, v1, s[4:5] offset:1024
	global_load_dword v3, v1, s[4:5]
	s_and_b32 s26, s2, 3
	s_bfe_u32 s27, s2, 0x30002
	s_lshl_b32 s36, s3, 20
	s_add_u32 s32, s28, s36
	s_addc_u32 s33, s29, 0
	s_lshl_b32 s36, s27, 17
	s_add_u32 s32, s32, s36
	s_addc_u32 s33, s33, 0
	s_lshl_b32 s36, s26, 9
	s_add_u32 s32, s32, s36
	s_addc_u32 s33, s33, 0
	s_lshl_b32 s36, s3, 11
	s_add_u32 s34, s16, s36
	s_addc_u32 s35, s17, 0
	s_lshl_b32 s36, s27, 8
	s_add_u32 s34, s34, s36
	s_addc_u32 s35, s35, 0
	v_lshrrev_b32_e32 v42, 5, v0
	v_and_b32_e32 v43, 31, v0
	v_lshlrev_b32_e32 v43, 4, v43
	v_lshl_or_b32 v43, v42, 11, v43
	v_lshlrev_b32_e32 v42, 2, v42
	global_load_dwordx4 v[52:55], v43, s[32:33]
	v_add_u32_e32 v84, 0x4000, v43
	global_load_dwordx4 v[56:59], v84, s[32:33]
	v_add_u32_e32 v84, 0x8000, v43
	global_load_dwordx4 v[60:63], v84, s[32:33]
	v_add_u32_e32 v84, 0xc000, v43
	global_load_dwordx4 v[64:67], v84, s[32:33]
	v_add_u32_e32 v84, 0x10000, v43
	global_load_dwordx4 v[68:71], v84, s[32:33]
	v_add_u32_e32 v84, 0x14000, v43
	global_load_dwordx4 v[72:75], v84, s[32:33]
	v_add_u32_e32 v84, 0x18000, v43
	global_load_dwordx4 v[76:79], v84, s[32:33]
	v_add_u32_e32 v84, 0x1c000, v43
	global_load_dwordx4 v[80:83], v84, s[32:33]
	global_load_dword v44, v42, s[34:35]
	global_load_dword v45, v42, s[34:35] offset:32
	global_load_dword v46, v42, s[34:35] offset:64
	global_load_dword v47, v42, s[34:35] offset:96
	global_load_dword v48, v42, s[34:35] offset:128
	global_load_dword v49, v42, s[34:35] offset:160
	global_load_dword v50, v42, s[34:35] offset:192
	global_load_dword v51, v42, s[34:35] offset:224
	v_mbcnt_lo_u32_b32 v1, -1, 0
	v_mbcnt_hi_u32_b32 v1, -1, v1
	v_and_b32_e32 v4, 64, v1
	v_xor_b32_e32 v5, 32, v1
	v_add_u32_e32 v4, 64, v4
	v_cmp_lt_i32_e32 vcc, v5, v4
	s_load_dwordx4 s[4:7], s[0:1], 0x0
	s_waitcnt vmcnt(17)
	v_mul_f32_e32 v2, v2, v2
	v_cndmask_b32_e32 v5, v1, v5, vcc
	v_lshlrev_b32_e32 v5, 2, v5
	s_waitcnt vmcnt(16)
	v_fmac_f32_e32 v2, v3, v3
	ds_bpermute_b32 v3, v5, v2
	v_xor_b32_e32 v5, 16, v1
	v_cmp_lt_i32_e32 vcc, v5, v4
	s_waitcnt lgkmcnt(0)
	v_add_f32_e32 v2, v2, v3
	v_cndmask_b32_e32 v5, v1, v5, vcc
	v_lshlrev_b32_e32 v5, 2, v5
	ds_bpermute_b32 v3, v5, v2
	v_xor_b32_e32 v5, 8, v1
	v_cmp_lt_i32_e32 vcc, v5, v4
	s_waitcnt lgkmcnt(0)
	v_add_f32_e32 v2, v2, v3
	v_cndmask_b32_e32 v5, v1, v5, vcc
	v_lshlrev_b32_e32 v5, 2, v5
	ds_bpermute_b32 v3, v5, v2
	v_xor_b32_e32 v5, 4, v1
	v_cmp_lt_i32_e32 vcc, v5, v4
	s_waitcnt lgkmcnt(0)
	v_add_f32_e32 v2, v2, v3
	v_cndmask_b32_e32 v5, v1, v5, vcc
	v_lshlrev_b32_e32 v5, 2, v5
	ds_bpermute_b32 v3, v5, v2
	v_xor_b32_e32 v5, 2, v1
	v_cmp_lt_i32_e32 vcc, v5, v4
	s_waitcnt lgkmcnt(0)
	v_add_f32_e32 v2, v2, v3
	v_cndmask_b32_e32 v5, v1, v5, vcc
	v_lshlrev_b32_e32 v5, 2, v5
	ds_bpermute_b32 v3, v5, v2
	v_xor_b32_e32 v5, 1, v1
	v_cmp_lt_i32_e32 vcc, v5, v4
	s_waitcnt lgkmcnt(0)
	v_add_f32_e32 v2, v2, v3
	v_cndmask_b32_e32 v1, v1, v5, vcc
	v_lshlrev_b32_e32 v1, 2, v1
	ds_bpermute_b32 v3, v1, v2
	v_and_b32_e32 v1, 63, v0
	v_cmp_eq_u32_e32 vcc, 0, v1
	s_and_saveexec_b64 s[0:1], vcc
	s_cbranch_execz .LBB0_77
	v_lshrrev_b32_e32 v4, 4, v0
	s_waitcnt lgkmcnt(0)
	v_add_f32_e32 v2, v2, v3
	ds_write_b32 v4, v2 offset:17408
.LBB0_77:
	s_or_b64 exec, exec, s[0:1]
	s_and_b32 s10, s2, 3
	s_bfe_u32 s2, s2, 0x30002
	s_lshl_b32 s11, s2, 6
	s_lshl_b32 s0, s3, 20
	s_add_u32 s0, s4, s0
	s_addc_u32 s1, s5, 0
	s_lshl_b32 s4, s2, 17
	s_add_u32 s0, s0, s4
	s_addc_u32 s1, s1, 0
	s_lshl_b32 s4, s10, 9
	s_add_u32 s0, s0, s4
	s_addc_u32 s1, s1, 0
	s_waitcnt lgkmcnt(0)
	v_mov_b32_e32 v3, 0
	s_or_b32 s8, s11, s8
	v_lshrrev_b32_e32 v28, 5, v0
	v_or_b32_e32 v4, s8, v28
	v_mov_b32_e32 v5, v3
	v_lshl_add_u64 v[4:5], v[4:5], 2, s[16:17]
	s_barrier
	s_waitcnt vmcnt(0)
	v_mov_b32_e32 v29, v44
	v_or_b32_e32 v14, 0x200, v0
	v_lshrrev_b32_e32 v33, 5, v14
	v_or_b32_e32 v2, 0x100, v0
	v_mov_b32_e32 v19, v3
	v_or_b32_e32 v18, s8, v33
	v_lshrrev_b32_e32 v30, 5, v2
	v_lshl_add_u64 v[18:19], v[18:19], 2, s[16:17]
	v_mov_b32_e32 v34, v46
	v_or_b32_e32 v4, s8, v30
	v_mov_b32_e32 v5, v3
	v_lshl_add_u64 v[4:5], v[4:5], 2, s[16:17]
	v_mov_b32_e32 v31, v45
	v_and_b32_e32 v20, 31, v0
	v_lshlrev_b32_e32 v2, 4, v20
	v_lshl_add_u64 v[4:5], s[0:1], 0, v[2:3]
	v_lshlrev_b32_e32 v2, 11, v28
	v_lshl_add_u64 v[6:7], v[4:5], 0, v[2:3]
	v_mov_b32_e32 v6, v52
	v_mov_b32_e32 v7, v53
	v_mov_b32_e32 v8, v54
	v_mov_b32_e32 v9, v55
	v_mov_b32_e32 v15, v3
	v_lshlrev_b32_e32 v14, 11, v30
	v_lshl_add_u64 v[14:15], v[4:5], 0, v[14:15]
	v_mov_b32_e32 v14, v56
	v_mov_b32_e32 v15, v57
	v_mov_b32_e32 v16, v58
	v_mov_b32_e32 v17, v59
	ds_read_b128 v[10:13], v3 offset:17408
	s_brev_b32 s11, 34
	v_or_b32_e32 v21, 0x300, v0
	v_lshrrev_b32_e32 v36, 5, v21
	v_mov_b32_e32 v19, v3
	s_waitcnt lgkmcnt(0)
	v_add_f32_e32 v10, v10, v11
	v_add_f32_e32 v10, v10, v12
	v_add_f32_e32 v37, v10, v13
	v_div_scale_f32 v38, s[0:1], v37, v37, s11
	v_rcp_f32_e32 v40, v38
	v_mov_b32_e32 v23, v3
	v_lshlrev_b32_e32 v18, 11, v33
	v_or_b32_e32 v22, s8, v36
	v_lshlrev_b32_e32 v35, 3, v20
	v_mov_b32_e32 v21, v3
	v_lshlrev_b32_e32 v20, 11, v36
	v_lshl_add_u64 v[24:25], v[4:5], 0, v[18:19]
	v_lshl_add_u64 v[22:23], v[22:23], 2, s[16:17]
	v_lshl_add_u64 v[26:27], v[4:5], 0, v[20:21]
	v_mov_b32_e32 v10, v60
	v_mov_b32_e32 v11, v61
	v_mov_b32_e32 v12, v62
	v_mov_b32_e32 v13, v63
	v_mov_b32_e32 v41, v47
	v_mov_b32_e32 v18, v64
	v_mov_b32_e32 v19, v65
	v_mov_b32_e32 v20, v66
	v_mov_b32_e32 v21, v67
	v_fma_f32 v22, -v38, v40, 1.0
	v_div_scale_f32 v39, vcc, s11, v37, s11
	v_fmac_f32_e32 v40, v22, v40
	v_mul_f32_e32 v22, v39, v40
	v_fma_f32 v23, -v38, v22, v39
	v_fmac_f32_e32 v22, v23, v40
	v_fma_f32 v23, -v38, v22, v39
	v_div_fmas_f32 v22, v23, v40, v22
	v_div_fixup_f32 v37, v22, v37, s11
	s_mov_b32 s5, 0x800000
	v_mov_b32_e32 v32, 0x42000000
	v_or_b32_e32 v2, 0x10000, v2
	s_mov_b32 s4, 0x39800000
	s_waitcnt vmcnt(7)
	v_mul_f32_e32 v22, v29, v29
	v_mul_f32_e32 v22, v37, v22
	v_max_f32_e32 v22, 0x2b8cbccc, v22
	v_cmp_gt_f32_e32 vcc, s5, v22
	s_waitcnt vmcnt(5)
	v_mul_f32_e32 v23, v31, v31
	v_cndmask_b32_e64 v24, 0, 32, vcc
	v_ldexp_f32 v22, v22, v24
	v_log_f32_e32 v22, v22
	v_mul_f32_e32 v23, v37, v23
	v_max_f32_e32 v23, 0x2b8cbccc, v23
	v_cndmask_b32_e32 v24, 0, v32, vcc
	v_cmp_gt_f32_e64 s[0:1], s5, v23
	v_sub_f32_e32 v22, v22, v24
	v_mul_f32_e32 v22, 0.5, v22
	v_cndmask_b32_e64 v25, 0, 32, s[0:1]
	v_ldexp_f32 v23, v23, v25
	v_rndne_f32_e32 v22, v22
	v_log_f32_e32 v25, v23
	v_cvt_i32_f32_e32 v24, v22
	v_lshl_add_u64 v[22:23], v[4:5], 0, v[2:3]
	v_cndmask_b32_e64 v2, 0, v32, s[0:1]
	v_sub_f32_e32 v25, v25, v2
	v_sub_u32_e32 v2, 0, v24
	v_med3_i32 v2, v2, -1, 3
	v_sub_u32_e32 v2, 0, v2
	v_ldexp_f32 v2, s4, v2
	s_waitcnt vmcnt(4)
	v_pk_mul_f32 v[6:7], v[6:7], v[2:3] op_sel_hi:[1,0]
	v_pk_mul_f32 v[8:9], v[8:9], v[2:3] op_sel_hi:[1,0]
	v_add_u32_e32 v2, s8, v28
	v_cvt_pk_f16_f32 v6, v6, v7
	v_cvt_pk_f16_f32 v7, v8, v9
	v_lshl_add_u64 v[8:9], v[2:3], 2, s[16:17]
	v_mov_b32_e32 v29, v48
	v_mul_f32_e32 v2, 0.5, v25
	v_rndne_f32_e32 v2, v2
	v_cvt_i32_f32_e32 v2, v2
	s_movk_i32 s0, 0x110
	v_mad_u32_u24 v28, v28, s0, v35
	ds_write_b64 v28, v[6:7]
	v_sub_u32_e32 v2, 0, v2
	v_med3_i32 v2, v2, -1, 3
	v_sub_u32_e32 v2, 0, v2
	v_ldexp_f32 v2, s4, v2
	s_waitcnt vmcnt(4)
	v_pk_mul_f32 v[6:7], v[14:15], v[2:3] op_sel_hi:[1,0]
	v_mul_f32_e32 v8, v34, v34
	v_cvt_pk_f16_f32 v14, v6, v7
	v_pk_mul_f32 v[6:7], v[16:17], v[2:3] op_sel_hi:[1,0]
	v_or_b32_e32 v2, 0x500, v0
	v_lshrrev_b32_e32 v31, 5, v2
	v_lshlrev_b32_e32 v2, 11, v31
	v_lshl_add_u64 v[16:17], v[4:5], 0, v[2:3]
	v_add_u32_e32 v2, s8, v31
	v_cvt_pk_f16_f32 v15, v6, v7
	v_lshl_add_u64 v[6:7], v[2:3], 2, s[16:17]
	v_mul_f32_e32 v2, v37, v8
	v_max_f32_e32 v2, 0x2b8cbccc, v2
	v_cmp_gt_f32_e32 vcc, s5, v2
	v_mov_b32_e32 v34, v49
	s_nop 0
	v_cndmask_b32_e64 v6, 0, 32, vcc
	v_ldexp_f32 v2, v2, v6
	v_log_f32_e32 v2, v2
	v_mov_b32_e32 v6, v68
	v_mov_b32_e32 v7, v69
	v_mov_b32_e32 v8, v70
	v_mov_b32_e32 v9, v71
	v_mad_u32_u24 v22, v30, s0, v35
	ds_write_b64 v22, v[14:15]
	v_cndmask_b32_e32 v14, 0, v32, vcc
	v_sub_f32_e32 v2, v2, v14
	v_mul_f32_e32 v2, 0.5, v2
	v_rndne_f32_e32 v2, v2
	v_cvt_i32_f32_e32 v26, v2
	v_or_b32_e32 v2, 0x600, v0
	v_lshrrev_b32_e32 v30, 5, v2
	v_lshlrev_b32_e32 v2, 11, v30
	v_lshl_add_u64 v[22:23], v[4:5], 0, v[2:3]
	v_add_u32_e32 v2, s8, v30
	v_lshl_add_u64 v[24:25], v[2:3], 2, s[16:17]
	v_sub_u32_e32 v2, 0, v26
	v_med3_i32 v2, v2, -1, 3
	v_sub_u32_e32 v2, 0, v2
	v_mov_b32_e32 v38, v50
	v_ldexp_f32 v2, s4, v2
	s_waitcnt vmcnt(6)
	v_pk_mul_f32 v[10:11], v[10:11], v[2:3] op_sel_hi:[1,0]
	v_pk_mul_f32 v[26:27], v[12:13], v[2:3] op_sel_hi:[1,0]
	s_waitcnt vmcnt(5)
	v_mul_f32_e32 v2, v41, v41
	v_mul_f32_e32 v2, v37, v2
	v_max_f32_e32 v2, 0x2b8cbccc, v2
	v_cmp_gt_f32_e32 vcc, s5, v2
	v_cvt_pk_f16_f32 v24, v10, v11
	v_mov_b32_e32 v14, v72
	v_mov_b32_e32 v15, v73
	v_mov_b32_e32 v16, v74
	v_mov_b32_e32 v17, v75
	v_cndmask_b32_e64 v10, 0, 32, vcc
	v_ldexp_f32 v2, v2, v10
	v_log_f32_e32 v25, v2
	v_or_b32_e32 v2, 0x700, v0
	v_lshrrev_b32_e32 v39, 5, v2
	v_lshlrev_b32_e32 v2, 11, v39
	v_lshl_add_u64 v[4:5], v[4:5], 0, v[2:3]
	v_add_u32_e32 v2, s8, v39
	v_mov_b32_e32 v10, v76
	v_mov_b32_e32 v11, v77
	v_mov_b32_e32 v12, v78
	v_mov_b32_e32 v13, v79
	v_lshl_add_u64 v[22:23], v[2:3], 2, s[16:17]
	v_mov_b32_e32 v40, v51
	v_cndmask_b32_e32 v2, 0, v32, vcc
	v_sub_f32_e32 v2, v25, v2
	v_cvt_pk_f16_f32 v25, v26, v27
	v_mad_u32_u24 v22, v33, s0, v35
	ds_write_b64 v22, v[24:25]
	v_mul_f32_e32 v2, 0.5, v2
	v_rndne_f32_e32 v2, v2
	v_cvt_i32_f32_e32 v2, v2
	v_sub_u32_e32 v2, 0, v2
	s_waitcnt vmcnt(6)
	v_mul_f32_e32 v22, v29, v29
	v_mul_f32_e32 v22, v37, v22
	v_max_f32_e32 v22, 0x2b8cbccc, v22
	v_cmp_gt_f32_e32 vcc, s5, v22
	v_med3_i32 v2, v2, -1, 3
	v_sub_u32_e32 v2, 0, v2
	v_cndmask_b32_e64 v23, 0, 32, vcc
	v_ldexp_f32 v22, v22, v23
	v_log_f32_e32 v26, v22
	v_mov_b32_e32 v22, v80
	v_mov_b32_e32 v23, v81
	v_mov_b32_e32 v24, v82
	v_mov_b32_e32 v25, v83
	v_ldexp_f32 v2, s4, v2
	v_pk_mul_f32 v[18:19], v[18:19], v[2:3] op_sel_hi:[1,0]
	s_nop 0
	v_cvt_pk_f16_f32 v4, v18, v19
	v_pk_mul_f32 v[18:19], v[20:21], v[2:3] op_sel_hi:[1,0]
	v_cndmask_b32_e32 v2, 0, v32, vcc
	v_sub_f32_e32 v2, v26, v2
	v_mul_f32_e32 v2, 0.5, v2
	v_rndne_f32_e32 v2, v2
	v_cvt_pk_f16_f32 v5, v18, v19
	v_mad_u32_u24 v18, v36, s0, v35
	v_cvt_i32_f32_e32 v2, v2
	ds_write_b64 v18, v[4:5]
	s_waitcnt vmcnt(6)
	v_mul_f32_e32 v4, v34, v34
	v_mul_f32_e32 v4, v37, v4
	v_max_f32_e32 v4, 0x2b8cbccc, v4
	v_cmp_gt_f32_e32 vcc, s5, v4
	v_sub_u32_e32 v2, 0, v2
	v_med3_i32 v2, v2, -1, 3
	v_cndmask_b32_e64 v5, 0, 32, vcc
	v_ldexp_f32 v4, v4, v5
	v_sub_u32_e32 v2, 0, v2
	v_log_f32_e32 v18, v4
	v_ldexp_f32 v2, s4, v2
	s_waitcnt vmcnt(5)
	v_pk_mul_f32 v[4:5], v[6:7], v[2:3] op_sel_hi:[1,0]
	v_pk_mul_f32 v[6:7], v[8:9], v[2:3] op_sel_hi:[1,0]
	v_cvt_pk_f16_f32 v4, v4, v5
	v_cndmask_b32_e32 v5, 0, v32, vcc
	v_sub_f32_e32 v5, v18, v5
	v_mul_f32_e32 v5, 0.5, v5
	v_rndne_f32_e32 v5, v5
	v_cvt_i32_f32_e32 v18, v5
	v_cvt_pk_f16_f32 v5, v6, v7
	ds_write_b64 v28, v[4:5] offset:8704
	s_waitcnt vmcnt(4)
	v_mul_f32_e32 v6, v38, v38
	v_mul_f32_e32 v6, v37, v6
	v_max_f32_e32 v6, 0x2b8cbccc, v6
	v_cmp_gt_f32_e32 vcc, s5, v6
	v_sub_u32_e32 v2, 0, v18
	v_med3_i32 v2, v2, -1, 3
	v_cndmask_b32_e64 v7, 0, 32, vcc
	v_ldexp_f32 v6, v6, v7
	v_log_f32_e32 v8, v6
	v_sub_u32_e32 v2, 0, v2
	v_ldexp_f32 v2, s4, v2
	s_waitcnt vmcnt(3)
	v_pk_mul_f32 v[4:5], v[14:15], v[2:3] op_sel_hi:[1,0]
	v_pk_mul_f32 v[6:7], v[16:17], v[2:3] op_sel_hi:[1,0]
	v_cndmask_b32_e32 v2, 0, v32, vcc
	v_sub_f32_e32 v2, v8, v2
	v_cvt_pk_f16_f32 v4, v4, v5
	v_mul_f32_e32 v2, 0.5, v2
	v_cvt_pk_f16_f32 v5, v6, v7
	v_mad_u32_u24 v6, v31, s0, v35
	v_rndne_f32_e32 v2, v2
	ds_write_b64 v6, v[4:5]
	s_waitcnt vmcnt(1)
	v_mul_f32_e32 v6, v40, v40
	v_cvt_i32_f32_e32 v2, v2
	v_mul_f32_e32 v6, v37, v6
	v_max_f32_e32 v6, 0x2b8cbccc, v6
	v_cmp_gt_f32_e32 vcc, s5, v6
	v_sub_u32_e32 v2, 0, v2
	v_med3_i32 v2, v2, -1, 3
	v_cndmask_b32_e64 v7, 0, 32, vcc
	v_ldexp_f32 v6, v6, v7
	v_log_f32_e32 v8, v6
	v_sub_u32_e32 v2, 0, v2
	v_ldexp_f32 v2, s4, v2
	v_pk_mul_f32 v[4:5], v[10:11], v[2:3] op_sel_hi:[1,0]
	v_pk_mul_f32 v[6:7], v[12:13], v[2:3] op_sel_hi:[1,0]
	v_cndmask_b32_e32 v2, 0, v32, vcc
	v_sub_f32_e32 v2, v8, v2
	v_mul_f32_e32 v2, 0.5, v2
	v_rndne_f32_e32 v2, v2
	v_cvt_i32_f32_e32 v2, v2
	v_cvt_pk_f16_f32 v4, v4, v5
	v_cvt_pk_f16_f32 v5, v6, v7
	v_mad_u32_u24 v6, v30, s0, v35
	v_sub_u32_e32 v2, 0, v2
	v_med3_i32 v2, v2, -1, 3
	v_sub_u32_e32 v2, 0, v2
	v_ldexp_f32 v2, s4, v2
	ds_write_b64 v6, v[4:5]
	s_waitcnt vmcnt(0)
	v_pk_mul_f32 v[4:5], v[22:23], v[2:3] op_sel_hi:[1,0]
	v_pk_mul_f32 v[6:7], v[24:25], v[2:3] op_sel_hi:[1,0]
	v_cvt_pk_f16_f32 v4, v4, v5
	v_cvt_pk_f16_f32 v5, v6, v7
	v_mad_u32_u24 v2, v39, s0, v35
	ds_write_b64 v2, v[4:5]
	v_lshrrev_b32_e32 v2, 6, v0
	v_and_b32_e32 v4, 15, v0
	v_lshl_or_b32 v4, v2, 4, v4
	v_and_b32_e32 v0, 48, v0
	v_mad_u32_u24 v12, v4, s0, v0
	s_lshl_b32 s0, s2, 12
	s_add_u32 s0, s6, s0
	s_addc_u32 s1, s7, 0
	v_lshlrev_b32_e32 v2, 10, v2
	v_lshl_add_u64 v[4:5], s[0:1], 0, v[2:3]
	v_lshlrev_b32_e32 v2, 4, v1
	s_waitcnt lgkmcnt(0)
	s_barrier
	v_lshl_add_u64 v[8:9], v[4:5], 0, v[2:3]
	ds_read_b128 v[0:3], v12
	ds_read_b128 v[4:7], v12 offset:64
	s_lshl_b32 s0, s3, 19
	s_lshl_b32 s1, s10, 17
	s_or_b32 s8, s0, s1
	v_lshl_add_u64 v[10:11], v[8:9], 0, s[8:9]
	s_or_b32 s0, s8, 0x8000
	s_mov_b32 s1, s9
	s_waitcnt lgkmcnt(1)
	global_store_dwordx4 v[10:11], v[0:3], off
	s_nop 1
	v_lshl_add_u64 v[0:1], v[8:9], 0, s[0:1]
	s_waitcnt lgkmcnt(0)
	global_store_dwordx4 v[0:1], v[4:7], off
	ds_read_b128 v[0:3], v12 offset:128
	ds_read_b128 v[4:7], v12 offset:192
	s_or_b32 s0, s8, 0x10000
	v_lshl_add_u64 v[10:11], v[8:9], 0, s[0:1]
	s_or_b32 s8, s8, 0x18000
	s_waitcnt lgkmcnt(1)
	global_store_dwordx4 v[10:11], v[0:3], off
	s_nop 1
	v_lshl_add_u64 v[0:1], v[8:9], 0, s[8:9]
	s_waitcnt lgkmcnt(0)
	global_store_dwordx4 v[0:1], v[4:7], off
	s_endpgm

	.amdhsa_kernel _Z11prep_kernelPKfPDv8_DF16_S0_S0_S0_S0_S0_S0_S0_S0_S0_S2_PfPDF16_S4_S3_
		.amdhsa_group_segment_fixed_size 17440
		.amdhsa_private_segment_fixed_size 0
		.amdhsa_kernarg_size 128
		.amdhsa_user_sgpr_count 2
		.amdhsa_user_sgpr_dispatch_ptr 0
		.amdhsa_user_sgpr_queue_ptr 0
		.amdhsa_user_sgpr_kernarg_segment_ptr 1
		.amdhsa_user_sgpr_dispatch_id 0
		.amdhsa_user_sgpr_kernarg_preload_length 0
		.amdhsa_user_sgpr_kernarg_preload_offset 0
		.amdhsa_user_sgpr_private_segment_size 0
		.amdhsa_uses_dynamic_stack 0
		.amdhsa_enable_private_segment 0
		.amdhsa_system_sgpr_workgroup_id_x 1
		.amdhsa_system_sgpr_workgroup_id_y 0
		.amdhsa_system_sgpr_workgroup_id_z 0
		.amdhsa_system_sgpr_workgroup_info 0
		.amdhsa_system_vgpr_workitem_id 0
		.amdhsa_next_free_vgpr 88
		.amdhsa_next_free_sgpr 40
		.amdhsa_accum_offset 88
		.amdhsa_reserve_vcc 1
		.amdhsa_float_round_mode_32 0
		.amdhsa_float_round_mode_16_64 0
		.amdhsa_float_denorm_mode_32 3
		.amdhsa_float_denorm_mode_16_64 3
		.amdhsa_dx10_clamp 1
		.amdhsa_ieee_mode 1
		.amdhsa_fp16_overflow 0
		.amdhsa_tg_split 0
		.amdhsa_exception_fp_ieee_invalid_op 0
		.amdhsa_exception_fp_denorm_src 0
		.amdhsa_exception_fp_ieee_div_zero 0
		.amdhsa_exception_fp_ieee_overflow 0
		.amdhsa_exception_fp_ieee_underflow 0
		.amdhsa_exception_fp_ieee_inexact 0
		.amdhsa_exception_int_div_zero 0
	.end_amdhsa_kernel

amdhsa.kernels:
  - .agpr_count:     0
    .args:
      - .actual_access:  read_only
        .address_space:  global
        .offset:         0
        .size:           8
        .value_kind:     global_buffer
      - .actual_access:  write_only
        .address_space:  global
        .offset:         8
        .size:           8
        .value_kind:     global_buffer
      - .actual_access:  read_only
        .address_space:  global
        .offset:         16
        .size:           8
        .value_kind:     global_buffer
      - .actual_access:  read_only
        .address_space:  global
        .offset:         24
        .size:           8
        .value_kind:     global_buffer
      - .actual_access:  read_only
        .address_space:  global
        .offset:         32
        .size:           8
        .value_kind:     global_buffer
      - .actual_access:  read_only
        .address_space:  global
        .offset:         40
        .size:           8
        .value_kind:     global_buffer
      - .actual_access:  read_only
        .address_space:  global
        .offset:         48
        .size:           8
        .value_kind:     global_buffer
      - .actual_access:  read_only
        .address_space:  global
        .offset:         56
        .size:           8
        .value_kind:     global_buffer
      - .actual_access:  read_only
        .address_space:  global
        .offset:         64
        .size:           8
        .value_kind:     global_buffer
      - .actual_access:  read_only
        .address_space:  global
        .offset:         72
        .size:           8
        .value_kind:     global_buffer
      - .actual_access:  read_only
        .address_space:  global
        .offset:         80
        .size:           8
        .value_kind:     global_buffer
      - .actual_access:  write_only
        .address_space:  global
        .offset:         88
        .size:           8
        .value_kind:     global_buffer
      - .actual_access:  write_only
        .address_space:  global
        .offset:         96
        .size:           8
        .value_kind:     global_buffer
      - .actual_access:  write_only
        .address_space:  global
        .offset:         104
        .size:           8
        .value_kind:     global_buffer
      - .actual_access:  write_only
        .address_space:  global
        .offset:         112
        .size:           8
        .value_kind:     global_buffer
      - .actual_access:  write_only
        .address_space:  global
        .offset:         120
        .size:           8
        .value_kind:     global_buffer
    .group_segment_fixed_size: 17440
    .kernarg_segment_align: 8
    .kernarg_segment_size: 128
    .language:       OpenCL C
    .language_version:
      - 2
      - 0
    .max_flat_workgroup_size: 256
    .name:           _Z11prep_kernelPKfPDv8_DF16_S0_S0_S0_S0_S0_S0_S0_S0_S0_S2_PfPDF16_S4_S3_
    .private_segment_fixed_size: 0
    .sgpr_count:     46
    .sgpr_spill_count: 0
    .symbol:         _Z11prep_kernelPKfPDv8_DF16_S0_S0_S0_S0_S0_S0_S0_S0_S0_S2_PfPDF16_S4_S3_.kd
    .uniform_work_group_size: 1
    .uses_dynamic_stack: false
    .vgpr_count:     88
    .vgpr_spill_count: 0
    .wavefront_size: 64
  - .agpr_count:     0
    .args:
      - .actual_access:  read_only
        .address_space:  global
        .offset:         0
        .size:           8
        .value_kind:     global_buffer
      - .actual_access:  read_only
        .address_space:  global
        .offset:         8
        .size:           8
        .value_kind:     global_buffer
      - .actual_access:  read_only
        .address_space:  global
        .offset:         16
        .size:           8
        .value_kind:     global_buffer
      - .actual_access:  read_only
        .address_space:  global
        .offset:         24
        .size:           8
        .value_kind:     global_buffer
      - .actual_access:  read_only
        .address_space:  global
        .offset:         32
        .size:           8
        .value_kind:     global_buffer
      - .actual_access:  read_only
        .address_space:  global
        .offset:         40
        .size:           8
        .value_kind:     global_buffer
      - .actual_access:  read_only
        .address_space:  global
        .offset:         48
        .size:           8
        .value_kind:     global_buffer
      - .actual_access:  read_only
        .address_space:  global
        .offset:         56
        .size:           8
        .value_kind:     global_buffer
      - .actual_access:  read_only
        .address_space:  global
        .offset:         64
        .size:           8
        .value_kind:     global_buffer
      - .actual_access:  write_only
        .address_space:  global
        .offset:         72
        .size:           8
        .value_kind:     global_buffer
    .group_segment_fixed_size: 130304
    .kernarg_segment_align: 8
    .kernarg_segment_size: 80
    .language:       OpenCL C
    .language_version:
      - 2
      - 0
    .max_flat_workgroup_size: 512
    .name:           _Z16pdag_main_kernelPKfS0_S0_PKDv8_DF16_S3_S0_PKDF16_S5_S0_Pf
    .private_segment_fixed_size: 0
    .sgpr_count:     72
    .sgpr_spill_count: 0
    .symbol:         _Z16pdag_main_kernelPKfS0_S0_PKDv8_DF16_S3_S0_PKDF16_S5_S0_Pf.kd
    .uniform_work_group_size: 1
    .uses_dynamic_stack: false
    .vgpr_count:     256
    .vgpr_spill_count: 0
    .wavefront_size: 64
